# grid barrier: L1 invalidate issued at arrival (overlaps the wait) instead of after the release is observed; on top of the combine-phase changes
# speedup vs baseline: 1.0259x; 1.0098x over previous
.LBB0_237:
	s_mov_b64 s[6:7], exec
	v_mbcnt_lo_u32_b32 v3, s6, 0
	v_mbcnt_hi_u32_b32 v3, s7, v3
	v_cmp_eq_u32_e32 vcc, 0, v3
	s_and_saveexec_b64 s[2:3], vcc
	s_cbranch_execz .LBB0_239
	v_readlane_b32 s8, v255, 11
	s_lshl_b32 s8, s8, 8
	v_readlane_b32 s10, v255, 9
	v_readlane_b32 s11, v255, 10
	s_add_u32 s8, s10, s8
	s_addc_u32 s9, s11, 0
	s_bcnt1_i32_b64 s6, s[6:7]
	v_mov_b32_e32 v5, 0x1000
	v_mov_b32_e32 v6, s6
	global_atomic_add v5, v5, v6, s[8:9] offset:1024 sc0
	buffer_inv sc1

.LBB0_252:
	s_or_b64 exec, exec, s[6:7]
	s_waitcnt vmcnt(0)
	s_waitcnt vmcnt(0)

.LBB0_270:
	s_or_b64 exec, exec, s[2:3]
	s_waitcnt vmcnt(0)
	s_waitcnt vmcnt(0)

.LBB0_836:
	s_mov_b64 s[16:17], exec
	v_mbcnt_lo_u32_b32 v3, s16, 0
	v_mbcnt_hi_u32_b32 v3, s17, v3
	v_cmp_eq_u32_e32 vcc, 0, v3
	s_and_saveexec_b64 s[6:7], vcc
	s_cbranch_execz .LBB0_838
	v_readlane_b32 s8, v255, 11
	s_lshl_b32 s8, s8, 8
	v_readlane_b32 s10, v255, 9
	v_readlane_b32 s11, v255, 10
	s_add_u32 s8, s10, s8
	s_addc_u32 s9, s11, 0
	s_bcnt1_i32_b64 s10, s[16:17]
	v_mov_b32_e32 v5, 0x1000
	v_mov_b32_e32 v6, s10
	global_atomic_add v5, v5, v6, s[8:9] offset:1024 sc0
	buffer_inv sc1

.LBB0_851:
	s_or_b64 exec, exec, s[16:17]
	s_waitcnt vmcnt(0)
	s_waitcnt vmcnt(0)

.LBB0_916:
	s_mov_b64 s[8:9], exec
	v_mbcnt_lo_u32_b32 v3, s8, 0
	v_mbcnt_hi_u32_b32 v3, s9, v3
	v_cmp_eq_u32_e32 vcc, 0, v3
	s_and_saveexec_b64 s[6:7], vcc
	s_cbranch_execz .LBB0_918
	v_readlane_b32 s10, v255, 11
	s_lshl_b32 s10, s10, 8
	v_readlane_b32 s14, v255, 9
	v_readlane_b32 s15, v255, 10
	s_add_u32 s10, s14, s10
	s_addc_u32 s11, s15, 0
	s_bcnt1_i32_b64 s8, s[8:9]
	v_mov_b32_e32 v5, 0x1000
	v_mov_b32_e32 v6, s8
	global_atomic_add v5, v5, v6, s[10:11] offset:1024 sc0
	buffer_inv sc1

.LBB0_931:
	s_or_b64 exec, exec, s[8:9]
	s_waitcnt vmcnt(0)
	s_waitcnt vmcnt(0)

.LBB0_996:
	s_mov_b64 s[8:9], exec
	v_mbcnt_lo_u32_b32 v67, s8, 0
	v_mbcnt_hi_u32_b32 v67, s9, v67
	v_cmp_eq_u32_e32 vcc, 0, v67
	s_and_saveexec_b64 s[6:7], vcc
	s_cbranch_execz .LBB0_998
	v_readlane_b32 s10, v255, 11
	s_lshl_b32 s10, s10, 8
	v_readlane_b32 s12, v255, 9
	v_readlane_b32 s13, v255, 10
	s_add_u32 s10, s12, s10
	s_addc_u32 s11, s13, 0
	s_bcnt1_i32_b64 s8, s[8:9]
	v_mov_b32_e32 v69, 0x1000
	v_mov_b32_e32 v70, s8
	global_atomic_add v69, v69, v70, s[10:11] offset:1024 sc0
	buffer_inv sc1

.LBB0_1136:
	s_mov_b64 s[6:7], exec
	v_mbcnt_lo_u32_b32 v3, s6, 0
	v_mbcnt_hi_u32_b32 v3, s7, v3
	v_cmp_eq_u32_e32 vcc, 0, v3
	s_and_saveexec_b64 s[4:5], vcc
	s_cbranch_execz .LBB0_1138
	v_readlane_b32 s8, v255, 11
	s_lshl_b32 s8, s8, 8
	v_readlane_b32 s10, v255, 9
	v_readlane_b32 s11, v255, 10
	s_add_u32 s8, s10, s8
	s_addc_u32 s9, s11, 0
	s_bcnt1_i32_b64 s6, s[6:7]
	v_mov_b32_e32 v5, 0x1000
	v_mov_b32_e32 v6, s6
	global_atomic_add v5, v5, v6, s[8:9] offset:1024 sc0
	buffer_inv sc1

.LBB0_1169:
	s_or_b64 exec, exec, s[4:5]
	s_waitcnt vmcnt(0)
	s_waitcnt vmcnt(0)

.LBB0_1249:
	s_mov_b64 s[6:7], exec
	v_mbcnt_lo_u32_b32 v3, s6, 0
	v_mbcnt_hi_u32_b32 v3, s7, v3
	v_cmp_eq_u32_e32 vcc, 0, v3
	s_and_saveexec_b64 s[2:3], vcc
	s_cbranch_execz .LBB0_1251
	v_readlane_b32 s8, v255, 11
	s_lshl_b32 s8, s8, 8
	v_readlane_b32 s12, v255, 9
	v_readlane_b32 s13, v255, 10
	s_add_u32 s8, s12, s8
	s_addc_u32 s9, s13, 0
	s_bcnt1_i32_b64 s6, s[6:7]
	v_mov_b32_e32 v5, 0x1000
	v_mov_b32_e32 v6, s6
	global_atomic_add v5, v5, v6, s[8:9] offset:1024 sc0
	buffer_inv sc1

.LBB0_1358:
	s_mov_b64 s[6:7], exec
	v_mbcnt_lo_u32_b32 v1, s6, 0
	v_mbcnt_hi_u32_b32 v1, s7, v1
	v_cmp_eq_u32_e32 vcc, 0, v1
	s_and_saveexec_b64 s[4:5], vcc
	s_cbranch_execz .LBB0_1360
	v_readlane_b32 s8, v255, 11
	s_lshl_b32 s8, s8, 8
	v_readlane_b32 s10, v255, 9
	v_readlane_b32 s11, v255, 10
	s_add_u32 s8, s10, s8
	s_addc_u32 s9, s11, 0
	s_bcnt1_i32_b64 s6, s[6:7]
	v_mov_b32_e32 v3, 0x1000
	v_mov_b32_e32 v4, s6
	global_atomic_add v3, v3, v4, s[8:9] offset:1024 sc0
	buffer_inv sc1
